# v57 + grid barrier release flattened: non-leader workgroups poll the cross-XCD generation word directly (skip the per-XCD leader relay hop)
# baseline (speedup 1.0000x reference)
.LBB0_340:
	v_readlane_b32 s4, v254, 11
	v_readlane_b32 s5, v254, 12
	v_cvt_f32_u32_e32 v1, v4
	v_sub_u32_e32 v6, 0, v4
	v_rcp_iflag_f32_e32 v1, v1
	s_nop 1
	global_atomic_add v5, v3, v208, s[4:5] sc0
	v_mul_f32_e32 v1, 0x4f7ffffe, v1
	v_cvt_u32_f32_e32 v1, v1
	v_mul_lo_u32 v6, v6, v1
	v_mul_hi_u32 v6, v1, v6
	v_add_u32_e32 v1, v1, v6
	s_waitcnt vmcnt(0)
	v_mul_hi_u32 v1, v5, v1
	v_mul_lo_u32 v6, v1, v4
	v_sub_u32_e32 v6, v5, v6
	v_add_u32_e32 v7, 1, v1
	v_cmp_ge_u32_e32 vcc, v6, v4
	v_add_u32_e32 v5, 1, v5
	s_nop 0
	v_cndmask_b32_e32 v1, v1, v7, vcc
	v_sub_u32_e32 v7, v6, v4
	v_cndmask_b32_e32 v6, v6, v7, vcc
	v_add_u32_e32 v7, 1, v1
	v_cmp_ge_u32_e32 vcc, v6, v4
	s_nop 1
	v_cndmask_b32_e32 v1, v1, v7, vcc
	v_mul_lo_u32 v6, v4, v1
	v_add_u32_e32 v4, v6, v4
	v_cmp_ne_u32_e32 vcc, v5, v4
	s_and_saveexec_b64 s[4:5], vcc
	s_xor_b64 s[4:5], exec, s[4:5]
	s_cbranch_execz .LBB0_354
	v_readlane_b32 s6, v254, 17
	v_readlane_b32 s7, v254, 18
	s_waitcnt lgkmcnt(0)
	s_nop 3
	global_load_dword v2, v3, s[6:7] sc1
	s_waitcnt vmcnt(0)
	v_cmp_eq_u32_e32 vcc, v2, v1
	s_and_saveexec_b64 s[6:7], vcc
	s_cbranch_execz .LBB0_353
	s_mov_b32 s21, 1
	s_mov_b64 s[8:9], 0
	s_branch .LBB0_344

.LBB0_1243:
	v_readlane_b32 s4, v254, 11
	v_readlane_b32 s5, v254, 12
	v_cvt_f32_u32_e32 v1, v4
	v_sub_u32_e32 v6, 0, v4
	v_rcp_iflag_f32_e32 v1, v1
	s_nop 1
	global_atomic_add v5, v3, v208, s[4:5] sc0
	v_mul_f32_e32 v1, 0x4f7ffffe, v1
	v_cvt_u32_f32_e32 v1, v1
	v_mul_lo_u32 v6, v6, v1
	v_mul_hi_u32 v6, v1, v6
	v_add_u32_e32 v1, v1, v6
	s_waitcnt vmcnt(0)
	v_mul_hi_u32 v1, v5, v1
	v_mul_lo_u32 v6, v1, v4
	v_sub_u32_e32 v6, v5, v6
	v_add_u32_e32 v7, 1, v1
	v_cmp_ge_u32_e32 vcc, v6, v4
	v_add_u32_e32 v5, 1, v5
	s_nop 0
	v_cndmask_b32_e32 v1, v1, v7, vcc
	v_sub_u32_e32 v7, v6, v4
	v_cndmask_b32_e32 v6, v6, v7, vcc
	v_add_u32_e32 v7, 1, v1
	v_cmp_ge_u32_e32 vcc, v6, v4
	s_nop 1
	v_cndmask_b32_e32 v1, v1, v7, vcc
	v_mul_lo_u32 v6, v4, v1
	v_add_u32_e32 v4, v6, v4
	v_cmp_ne_u32_e32 vcc, v5, v4
	s_and_saveexec_b64 s[4:5], vcc
	s_xor_b64 s[4:5], exec, s[4:5]
	s_cbranch_execz .LBB0_1257
	v_readlane_b32 s6, v254, 17
	v_readlane_b32 s7, v254, 18
	s_waitcnt lgkmcnt(0)
	s_nop 3
	global_load_dword v2, v3, s[6:7] sc1
	s_waitcnt vmcnt(0)
	v_cmp_eq_u32_e32 vcc, v2, v1
	s_and_saveexec_b64 s[6:7], vcc
	s_cbranch_execz .LBB0_1256
	s_mov_b32 s13, 1
	s_mov_b64 s[8:9], 0
	s_branch .LBB0_1247
